# P0 xbf loop rewritten by hand: two 16-B/lane XN stores per token (even/odd lanes take adjacent chunks, halves exchanged by DPP) instead of four 8-B/lane
# baseline (speedup 1.0000x reference)
.LBB0_50:
	s_or_b64 exec, exec, s[8:9]
	s_cmp_gt_i32 s14, 0xffff
	v_mbcnt_lo_u32_b32 v1, -1, 0
	s_cbranch_scc1 .LBB0_55
	v_mbcnt_hi_u32_b32 v2, -1, v1
	v_and_b32_e32 v3, 64, v2
	v_add_u32_e32 v3, 64, v3
	v_xor_b32_e32 v4, 1, v2
	v_cmp_lt_i32_e32 vcc, v4, v3
	s_load_dwordx2 s[2:3], s[16:17], 0x0
	s_ashr_i32 s15, s14, 31
	v_cndmask_b32_e32 v4, v2, v4, vcc
	v_lshlrev_b32_e32 v8, 2, v4
	v_xor_b32_e32 v4, 2, v2
	v_cmp_lt_i32_e32 vcc, v4, v3
	s_lshl_b64 s[0:1], s[14:15], 2
	s_add_u32 s0, s0, 0x80000
	v_cndmask_b32_e32 v4, v2, v4, vcc
	v_lshlrev_b32_e32 v9, 2, v4
	v_xor_b32_e32 v4, 4, v2
	v_cmp_lt_i32_e32 vcc, v4, v3
	s_addc_u32 s1, s1, 0
	s_ashr_i32 s81, s80, 31
	v_cndmask_b32_e32 v4, v2, v4, vcc
	v_lshlrev_b32_e32 v10, 2, v4
	v_xor_b32_e32 v4, 8, v2
	v_cmp_lt_i32_e32 vcc, v4, v3
	s_lshl_b64 s[6:7], s[14:15], 11
	s_lshl_b64 s[8:9], s[80:81], 2
	v_cndmask_b32_e32 v4, v2, v4, vcc
	v_lshlrev_b32_e32 v11, 2, v4
	v_xor_b32_e32 v4, 16, v2
	v_cmp_lt_i32_e32 vcc, v4, v3
	s_lshl_b64 s[10:11], s[80:81], 11
	v_mov_b32_e32 v5, 0
	v_cndmask_b32_e32 v4, v2, v4, vcc
	v_lshlrev_b32_e32 v12, 2, v4
	v_xor_b32_e32 v4, 32, v2
	v_cmp_lt_i32_e32 vcc, v4, v3
	v_mov_b32_e32 v3, s7
	v_cmp_eq_u32_e64 s[4:5], 0, v36
	v_cndmask_b32_e32 v2, v2, v4, vcc
	v_lshlrev_b32_e32 v13, 2, v2
	v_lshl_or_b32 v2, v36, 3, s6
	s_lshl_b64 s[6:7], s[14:15], 12
	s_waitcnt lgkmcnt(0)
	s_add_u32 s2, s2, s6
	v_lshlrev_b32_e32 v4, 4, v36
	s_addc_u32 s3, s3, s7
	v_lshl_add_u64 v[6:7], s[2:3], 0, v[4:5]
	s_mov_b64 s[2:3], 0x800
	v_lshl_add_u64 v[6:7], v[6:7], 0, s[2:3]
	s_lshl_b64 s[16:17], s[80:81], 12
	s_movk_i32 s2, 0x7fff
	s_mov_b32 s3, 0xffff0000
	s_mov_b32 s15, 0xdc00000
	v_mov_b32_e32 v4, 0x3727c5ac
	s_mov_b32 s20, 0xf800000
	v_mov_b32_e32 v14, 0x260
	s_mov_b32 s22, 0xaaaaaaaa
	s_mov_b32 s23, 0xaaaaaaaa
	v_and_b32_e32 v60, 1, v36
	v_mul_u32_u24_e32 v60, 0x1f8, v60
	v_add_u32_e32 v2, v2, v60
	s_branch .LBB0_53

.LBB0_53:
	s_waitcnt lgkmcnt(0)
	global_load_dwordx4 v[16:19], v[6:7], off offset:-2048
	global_load_dwordx4 v[20:23], v[6:7], off offset:-1024
	global_load_dwordx4 v[24:27], v[6:7], off
	global_load_dwordx4 v[28:31], v[6:7], off offset:1024
	v_lshl_add_u64 v[32:33], s[12:13], 0, v[2:3]
	v_add_co_u32_e32 v32, vcc, s15, v32
	s_nop 0
	v_addc_co_u32_e32 v33, vcc, 0, v33, vcc
	s_waitcnt vmcnt(3)
	v_mul_f32_e32 v15, v17, v17
	s_waitcnt vmcnt(2)
	v_mul_f32_e32 v34, v21, v21
	s_waitcnt vmcnt(1)
	v_mul_f32_e32 v35, v25, v25
	v_fmac_f32_e32 v34, v20, v20
	v_fmac_f32_e32 v15, v16, v16
	s_waitcnt vmcnt(0)
	v_mul_f32_e32 v36, v29, v29
	v_fmac_f32_e32 v35, v24, v24
	v_fmac_f32_e32 v34, v22, v22
	v_fmac_f32_e32 v15, v18, v18
	v_fmac_f32_e32 v36, v28, v28
	v_fmac_f32_e32 v35, v26, v26
	v_fmac_f32_e32 v34, v23, v23
	v_fmac_f32_e32 v15, v19, v19
	v_fmac_f32_e32 v36, v30, v30
	v_fmac_f32_e32 v35, v27, v27
	v_add_f32_e32 v15, v15, v34
	v_fmac_f32_e32 v36, v31, v31
	v_add_f32_e32 v15, v15, v35
	v_add_f32_e32 v15, v15, v36
	ds_bpermute_b32 v62, v8, v15
	v_bfe_u32 v37, v16, 16, 1
	v_bfe_u32 v38, v17, 16, 1
	v_add3_u32 v37, v16, v37, s2
	v_add3_u32 v38, v17, v38, s2
	v_lshrrev_b32_e32 v37, 16, v37
	v_and_or_b32 v40, v38, s3, v37
	v_bfe_u32 v39, v18, 16, 1
	v_bfe_u32 v48, v19, 16, 1
	v_add3_u32 v39, v18, v39, s2
	v_add3_u32 v48, v19, v48, s2
	v_lshrrev_b32_e32 v39, 16, v39
	v_and_or_b32 v41, v48, s3, v39
	s_waitcnt lgkmcnt(0)
	v_add_f32_e32 v15, v15, v62
	ds_bpermute_b32 v62, v9, v15
	v_bfe_u32 v37, v20, 16, 1
	v_bfe_u32 v38, v21, 16, 1
	v_add3_u32 v37, v20, v37, s2
	v_add3_u32 v38, v21, v38, s2
	v_lshrrev_b32_e32 v37, 16, v37
	v_and_or_b32 v42, v38, s3, v37
	v_bfe_u32 v39, v22, 16, 1
	v_bfe_u32 v48, v23, 16, 1
	v_add3_u32 v39, v22, v39, s2
	v_add3_u32 v48, v23, v48, s2
	v_lshrrev_b32_e32 v39, 16, v39
	v_and_or_b32 v43, v48, s3, v39
	s_waitcnt lgkmcnt(0)
	v_add_f32_e32 v15, v15, v62
	ds_bpermute_b32 v62, v10, v15
	v_cndmask_b32_e64 v49, v42, v40, s[22:23]
	v_cndmask_b32_e64 v50, v43, v41, s[22:23]
	s_nop 1
	v_mov_b32_dpp v51, v49 quad_perm:[1,0,3,2] row_mask:0xf bank_mask:0xf
	v_mov_b32_dpp v52, v50 quad_perm:[1,0,3,2] row_mask:0xf bank_mask:0xf
	s_nop 0
	v_cndmask_b32_e64 v54, v40, v51, s[22:23]
	v_cndmask_b32_e64 v55, v41, v52, s[22:23]
	v_cndmask_b32_e64 v56, v51, v42, s[22:23]
	v_cndmask_b32_e64 v57, v52, v43, s[22:23]
	global_store_dwordx4 v[32:33], v[54:57], off
	s_waitcnt lgkmcnt(0)
	v_add_f32_e32 v15, v15, v62
	ds_bpermute_b32 v62, v11, v15
	v_bfe_u32 v37, v24, 16, 1
	v_bfe_u32 v38, v25, 16, 1
	v_add3_u32 v37, v24, v37, s2
	v_add3_u32 v38, v25, v38, s2
	v_lshrrev_b32_e32 v37, 16, v37
	v_and_or_b32 v44, v38, s3, v37
	v_bfe_u32 v39, v26, 16, 1
	v_bfe_u32 v48, v27, 16, 1
	v_add3_u32 v39, v26, v39, s2
	v_add3_u32 v48, v27, v48, s2
	v_lshrrev_b32_e32 v39, 16, v39
	v_and_or_b32 v45, v48, s3, v39
	s_waitcnt lgkmcnt(0)
	v_add_f32_e32 v15, v15, v62
	ds_bpermute_b32 v62, v12, v15
	v_bfe_u32 v37, v28, 16, 1
	v_bfe_u32 v38, v29, 16, 1
	v_add3_u32 v37, v28, v37, s2
	v_add3_u32 v38, v29, v38, s2
	v_lshrrev_b32_e32 v37, 16, v37
	v_and_or_b32 v46, v38, s3, v37
	v_bfe_u32 v39, v30, 16, 1
	v_bfe_u32 v48, v31, 16, 1
	v_add3_u32 v39, v30, v39, s2
	v_add3_u32 v48, v31, v48, s2
	v_lshrrev_b32_e32 v39, 16, v39
	v_and_or_b32 v47, v48, s3, v39
	s_waitcnt lgkmcnt(0)
	v_add_f32_e32 v15, v15, v62
	ds_bpermute_b32 v16, v13, v15
	v_cndmask_b32_e64 v49, v46, v44, s[22:23]
	v_cndmask_b32_e64 v50, v47, v45, s[22:23]
	s_nop 1
	v_mov_b32_dpp v51, v49 quad_perm:[1,0,3,2] row_mask:0xf bank_mask:0xf
	v_mov_b32_dpp v52, v50 quad_perm:[1,0,3,2] row_mask:0xf bank_mask:0xf
	s_nop 0
	v_cndmask_b32_e64 v58, v44, v51, s[22:23]
	v_cndmask_b32_e64 v59, v45, v52, s[22:23]
	v_cndmask_b32_e64 v60, v51, v46, s[22:23]
	v_cndmask_b32_e64 v61, v52, v47, s[22:23]
	global_store_dwordx4 v[32:33], v[58:61], off offset:1024
	s_and_saveexec_b64 s[18:19], s[4:5]
	s_cbranch_execz .LBB0_52
	s_waitcnt lgkmcnt(0)
	v_add_f32_e32 v15, v15, v16
	v_fmamk_f32 v15, v15, 0x3a800000, v4
	v_mul_f32_e32 v16, 0x4f800000, v15
	v_cmp_gt_f32_e32 vcc, s20, v15
	s_nop 1
	v_cndmask_b32_e32 v15, v15, v16, vcc
	v_sqrt_f32_e32 v16, v15
	s_nop 0
	v_add_u32_e32 v17, -1, v16
	v_fma_f32 v19, -v17, v16, v15
	v_add_u32_e32 v18, 1, v16
	v_cmp_ge_f32_e64 s[6:7], 0, v19
	s_nop 1
	v_cndmask_b32_e64 v17, v16, v17, s[6:7]
	v_fma_f32 v16, -v18, v16, v15
	v_cmp_lt_f32_e64 s[6:7], 0, v16
	s_nop 1
	v_cndmask_b32_e64 v16, v17, v18, s[6:7]
	v_mul_f32_e32 v17, 0x37800000, v16
	v_cndmask_b32_e32 v16, v16, v17, vcc
	v_cmp_class_f32_e32 vcc, v15, v14
	s_nop 1
	v_cndmask_b32_e32 v15, v16, v15, vcc
	v_div_scale_f32 v16, s[6:7], v15, v15, 1.0
	v_rcp_f32_e32 v17, v16
	s_add_u32 s6, s12, s0
	s_addc_u32 s7, s13, s1
	v_fma_f32 v18, -v16, v17, 1.0
	v_fmac_f32_e32 v17, v18, v17
	v_div_scale_f32 v18, vcc, 1.0, v15, 1.0
	v_mul_f32_e32 v19, v18, v17
	v_fma_f32 v20, -v16, v19, v18
	v_fmac_f32_e32 v19, v20, v17
	v_fma_f32 v16, -v16, v19, v18
	v_div_fmas_f32 v16, v16, v17, v19
	v_div_fixup_f32 v15, v16, v15, 1.0
	global_store_dword v5, v15, s[6:7]
	s_branch .LBB0_52
